# spatial: exp/store VALU of block b interleaved into the MFMA gaps of block b+1 QK (pass 2 and the two recomputed blocks)
# baseline (speedup 1.0000x reference)
_Z9k_spatialPKDF16_S0_S0_PfPDF16_:
	s_load_dwordx4 s[4:7], s[0:1], 0x0
	s_load_dwordx2 s[10:11], s[0:1], 0x10
	s_mul_hi_i32 s9, s2, 0x3140
	s_mul_i32 s8, s2, 0x3140
	s_lshl_b64 s[8:9], s[8:9], 1
	v_and_b32_e32 v2, 7, v0
	v_lshrrev_b32_e32 v3, 3, v0
	v_lshlrev_b32_e32 v10, 4, v2
	v_lshl_or_b32 v4, v3, 7, v10
	v_add_u32_e32 v5, 0x1c00, v4
	v_add_u32_e32 v6, 0x3800, v4
	v_add_u32_e32 v7, 0x5400, v4
	v_lshrrev_b32_e32 v8, 1, v0
	v_and_b32_e32 v108, 31, v0
	v_and_b32_e32 v115, 0xe0, v8
	v_or_b32_e32 v109, v115, v108
	s_movk_i32 s3, 0xc5
	v_mov_b32_e32 v8, 0xc4
	v_cmp_gt_u32_e64 s[12:13], s3, v109
	v_bfe_u32 v1, v0, 5, 1
	v_lshlrev_b32_e32 v111, 4, v1
	s_nop 1
	v_cndmask_b32_e64 v110, v8, v109, s[12:13]
	v_lshl_or_b32 v9, v110, 7, v111
	s_movk_i32 s3, 0xe8
	v_cmp_gt_u32_e32 vcc, s3, v0
	v_or_b32_e32 v14, 0x6200, v10
	s_nop 1
	v_cndmask_b32_e32 v7, v14, v7, vcc
	s_waitcnt lgkmcnt(0)
	s_add_u32 s6, s6, s8
	s_addc_u32 s7, s7, s9
	s_add_u32 s10, s10, s8
	s_addc_u32 s11, s11, s9
	s_add_u32 s4, s4, s8
	s_addc_u32 s5, s5, s9
	global_load_dwordx4 v[18:21], v4, s[6:7] nt
	global_load_dwordx4 v[22:25], v4, s[10:11] nt
	global_load_dwordx4 v[26:29], v5, s[6:7] nt
	global_load_dwordx4 v[30:33], v5, s[10:11] nt
	global_load_dwordx4 v[34:37], v6, s[6:7] nt
	global_load_dwordx4 v[38:41], v6, s[10:11] nt
	global_load_dwordx4 v[42:45], v7, s[6:7] nt
	global_load_dwordx4 v[46:49], v7, s[10:11] nt
	global_load_dwordx4 v[74:77], v9, s[4:5] offset:0 nt
	global_load_dwordx4 v[78:81], v9, s[4:5] offset:32 nt
	global_load_dwordx4 v[82:85], v9, s[4:5] offset:64 nt
	global_load_dwordx4 v[86:89], v9, s[4:5] offset:96 nt
	s_movk_i32 s3, 0x90
	v_lshlrev_b32_e32 v11, 3, v2
	v_mul_u32_u24_e32 v16, 0x1c8, v11
	v_mad_u32_u24 v12, v3, s3, v10
	v_lshl_add_u32 v13, v3, 1, v16
	v_mad_u32_u24 v112, v108, s3, v111
	s_waitcnt vmcnt(11)
	ds_write_b128 v12, v[18:21] offset:0
	s_waitcnt vmcnt(10)
	ds_write_b16 v13, v22 offset:32256
	ds_write_b16_d16_hi v13, v22 offset:32712
	ds_write_b16 v13, v23 offset:33168
	ds_write_b16_d16_hi v13, v23 offset:33624
	ds_write_b16 v13, v24 offset:34080
	ds_write_b16_d16_hi v13, v24 offset:34536
	ds_write_b16 v13, v25 offset:34992
	ds_write_b16_d16_hi v13, v25 offset:35448
	s_waitcnt vmcnt(9)
	ds_write_b128 v12, v[26:29] offset:8064
	s_waitcnt vmcnt(8)
	ds_write_b16 v13, v30 offset:32368
	ds_write_b16_d16_hi v13, v30 offset:32824
	ds_write_b16 v13, v31 offset:33280
	ds_write_b16_d16_hi v13, v31 offset:33736
	ds_write_b16 v13, v32 offset:34192
	ds_write_b16_d16_hi v13, v32 offset:34648
	ds_write_b16 v13, v33 offset:35104
	ds_write_b16_d16_hi v13, v33 offset:35560
	s_waitcnt vmcnt(7)
	ds_write_b128 v12, v[34:37] offset:16128
	s_waitcnt vmcnt(6)
	ds_write_b16 v13, v38 offset:32480
	ds_write_b16_d16_hi v13, v38 offset:32936
	ds_write_b16 v13, v39 offset:33392
	ds_write_b16_d16_hi v13, v39 offset:33848
	ds_write_b16 v13, v40 offset:34304
	ds_write_b16_d16_hi v13, v40 offset:34760
	ds_write_b16 v13, v41 offset:35216
	ds_write_b16_d16_hi v13, v41 offset:35672
	s_waitcnt vmcnt(5)
	v_cndmask_b32_e32 v42, 0, v42, vcc
	v_cndmask_b32_e32 v43, 0, v43, vcc
	v_cndmask_b32_e32 v44, 0, v44, vcc
	v_cndmask_b32_e32 v45, 0, v45, vcc
	ds_write_b128 v12, v[42:45] offset:24192
	s_waitcnt vmcnt(4)
	v_cndmask_b32_e32 v46, 0, v46, vcc
	v_cndmask_b32_e32 v47, 0, v47, vcc
	v_cndmask_b32_e32 v48, 0, v48, vcc
	v_cndmask_b32_e32 v49, 0, v49, vcc
	ds_write_b16 v13, v46 offset:32592
	ds_write_b16_d16_hi v13, v46 offset:33048
	ds_write_b16 v13, v47 offset:33504
	ds_write_b16_d16_hi v13, v47 offset:33960
	ds_write_b16 v13, v48 offset:34416
	ds_write_b16_d16_hi v13, v48 offset:34872
	ds_write_b16 v13, v49 offset:35328
	ds_write_b16_d16_hi v13, v49 offset:35784
	s_load_dwordx2 s[8:9], s[0:1], 0x20
	s_load_dwordx2 s[10:11], s[0:1], 0x18
	s_mov_b32 s16, 0x3e38aa3b
	s_mov_b32 s17, 0xf149f2ca
	v_cmp_eq_u32_e64 s[14:15], 0, v1
	v_mul_u32_u24_e32 v113, 0x1c8, v108
	v_lshl_add_u32 v113, v1, 3, v113
	v_add_u32_e32 v113, 0x7e00, v113
	v_add_u32_e32 v114, 0x3900, v113
	v_mov_b32_e32 v106, s17
	s_waitcnt vmcnt(0) lgkmcnt(0)
	s_barrier
	ds_read_b128 v[66:69], v112 offset:0
	ds_read_b128 v[70:73], v112 offset:32
	s_waitcnt lgkmcnt(1)
	v_mfma_f32_32x32x16_f16 v[2:17], v[66:69], v[74:77], 0
	ds_read_b128 v[66:69], v112 offset:64
	s_waitcnt lgkmcnt(1)
	v_mfma_f32_32x32x16_f16 v[2:17], v[70:73], v[78:81], v[2:17]
	ds_read_b128 v[70:73], v112 offset:96
	s_waitcnt lgkmcnt(1)
	v_mfma_f32_32x32x16_f16 v[2:17], v[66:69], v[82:85], v[2:17]
	s_waitcnt lgkmcnt(0)
	v_mfma_f32_32x32x16_f16 v[2:17], v[70:73], v[86:89], v[2:17]
	ds_read_b128 v[66:69], v112 offset:4608
	ds_read_b128 v[70:73], v112 offset:4640
	s_waitcnt lgkmcnt(1)
	v_mfma_f32_32x32x16_f16 v[50:65], v[66:69], v[74:77], 0
	ds_read_b128 v[66:69], v112 offset:4672
	s_waitcnt lgkmcnt(1)
	v_mfma_f32_32x32x16_f16 v[50:65], v[70:73], v[78:81], v[50:65]
	ds_read_b128 v[70:73], v112 offset:4704
	s_waitcnt lgkmcnt(1)
	v_mfma_f32_32x32x16_f16 v[50:65], v[66:69], v[82:85], v[50:65]
	s_waitcnt lgkmcnt(0)
	v_mfma_f32_32x32x16_f16 v[50:65], v[70:73], v[86:89], v[50:65]
	v_max3_f32 v106, v106, v2, v3
	v_max3_f32 v106, v106, v4, v5
	v_max3_f32 v106, v106, v6, v7
	v_max3_f32 v106, v106, v8, v9
	v_max3_f32 v106, v106, v10, v11
	v_max3_f32 v106, v106, v12, v13
	v_max3_f32 v106, v106, v14, v15
	v_max3_f32 v106, v106, v16, v17
	ds_read_b128 v[66:69], v112 offset:9216
	ds_read_b128 v[70:73], v112 offset:9248
	s_waitcnt lgkmcnt(1)
	v_mfma_f32_32x32x16_f16 v[2:17], v[66:69], v[74:77], 0
	ds_read_b128 v[66:69], v112 offset:9280
	s_waitcnt lgkmcnt(1)
	v_mfma_f32_32x32x16_f16 v[2:17], v[70:73], v[78:81], v[2:17]
	ds_read_b128 v[70:73], v112 offset:9312
	s_waitcnt lgkmcnt(1)
	v_mfma_f32_32x32x16_f16 v[2:17], v[66:69], v[82:85], v[2:17]
	s_waitcnt lgkmcnt(0)
	v_mfma_f32_32x32x16_f16 v[2:17], v[70:73], v[86:89], v[2:17]
	v_max3_f32 v106, v106, v50, v51
	v_max3_f32 v106, v106, v52, v53
	v_max3_f32 v106, v106, v54, v55
	v_max3_f32 v106, v106, v56, v57
	v_max3_f32 v106, v106, v58, v59
	v_max3_f32 v106, v106, v60, v61
	v_max3_f32 v106, v106, v62, v63
	v_max3_f32 v106, v106, v64, v65
	ds_read_b128 v[66:69], v112 offset:13824
	ds_read_b128 v[70:73], v112 offset:13856
	s_waitcnt lgkmcnt(1)
	v_mfma_f32_32x32x16_f16 v[50:65], v[66:69], v[74:77], 0
	ds_read_b128 v[66:69], v112 offset:13888
	s_waitcnt lgkmcnt(1)
	v_mfma_f32_32x32x16_f16 v[50:65], v[70:73], v[78:81], v[50:65]
	ds_read_b128 v[70:73], v112 offset:13920
	s_waitcnt lgkmcnt(1)
	v_mfma_f32_32x32x16_f16 v[50:65], v[66:69], v[82:85], v[50:65]
	s_waitcnt lgkmcnt(0)
	v_mfma_f32_32x32x16_f16 v[50:65], v[70:73], v[86:89], v[50:65]
	v_max3_f32 v106, v106, v2, v3
	v_max3_f32 v106, v106, v4, v5
	v_max3_f32 v106, v106, v6, v7
	v_max3_f32 v106, v106, v8, v9
	v_max3_f32 v106, v106, v10, v11
	v_max3_f32 v106, v106, v12, v13
	v_max3_f32 v106, v106, v14, v15
	v_max3_f32 v106, v106, v16, v17
	ds_read_b128 v[66:69], v112 offset:18432
	ds_read_b128 v[70:73], v112 offset:18464
	s_waitcnt lgkmcnt(1)
	v_mfma_f32_32x32x16_f16 v[18:33], v[66:69], v[74:77], 0
	ds_read_b128 v[66:69], v112 offset:18496
	s_waitcnt lgkmcnt(1)
	v_mfma_f32_32x32x16_f16 v[18:33], v[70:73], v[78:81], v[18:33]
	ds_read_b128 v[70:73], v112 offset:18528
	s_waitcnt lgkmcnt(1)
	v_mfma_f32_32x32x16_f16 v[18:33], v[66:69], v[82:85], v[18:33]
	s_waitcnt lgkmcnt(0)
	v_mfma_f32_32x32x16_f16 v[18:33], v[70:73], v[86:89], v[18:33]
	v_max3_f32 v106, v106, v50, v51
	v_max3_f32 v106, v106, v52, v53
	v_max3_f32 v106, v106, v54, v55
	v_max3_f32 v106, v106, v56, v57
	v_max3_f32 v106, v106, v58, v59
	v_max3_f32 v106, v106, v60, v61
	v_max3_f32 v106, v106, v62, v63
	v_max3_f32 v106, v106, v64, v65
	ds_read_b128 v[66:69], v112 offset:23040
	ds_read_b128 v[70:73], v112 offset:23072
	s_waitcnt lgkmcnt(1)
	v_mfma_f32_32x32x16_f16 v[34:49], v[66:69], v[74:77], 0
	ds_read_b128 v[66:69], v112 offset:23104
	s_waitcnt lgkmcnt(1)
	v_mfma_f32_32x32x16_f16 v[34:49], v[70:73], v[78:81], v[34:49]
	ds_read_b128 v[70:73], v112 offset:23136
	s_waitcnt lgkmcnt(1)
	v_mfma_f32_32x32x16_f16 v[34:49], v[66:69], v[82:85], v[34:49]
	s_waitcnt lgkmcnt(0)
	v_mfma_f32_32x32x16_f16 v[34:49], v[70:73], v[86:89], v[34:49]
	v_max3_f32 v106, v106, v18, v19
	v_max3_f32 v106, v106, v20, v21
	v_max3_f32 v106, v106, v22, v23
	v_max3_f32 v106, v106, v24, v25
	v_max3_f32 v106, v106, v26, v27
	v_max3_f32 v106, v106, v28, v29
	v_max3_f32 v106, v106, v30, v31
	v_max3_f32 v106, v106, v32, v33
	ds_read_b128 v[66:69], v112 offset:27648
	ds_read_b128 v[70:73], v112 offset:27680
	s_waitcnt lgkmcnt(1)
	v_mfma_f32_32x32x16_f16 v[90:105], v[66:69], v[74:77], 0
	ds_read_b128 v[66:69], v112 offset:27712
	s_waitcnt lgkmcnt(1)
	v_mfma_f32_32x32x16_f16 v[90:105], v[70:73], v[78:81], v[90:105]
	ds_read_b128 v[70:73], v112 offset:27744
	s_waitcnt lgkmcnt(1)
	v_mfma_f32_32x32x16_f16 v[90:105], v[66:69], v[82:85], v[90:105]
	s_waitcnt lgkmcnt(0)
	v_mfma_f32_32x32x16_f16 v[90:105], v[70:73], v[86:89], v[90:105]
	v_max3_f32 v106, v106, v34, v35
	v_max3_f32 v106, v106, v36, v37
	v_max3_f32 v106, v106, v38, v39
	v_max3_f32 v106, v106, v40, v41
	v_max3_f32 v106, v106, v42, v43
	v_max3_f32 v106, v106, v44, v45
	v_max3_f32 v106, v106, v46, v47
	v_max3_f32 v106, v106, v48, v49
	s_nop 15
	s_nop 1
	v_mov_b32_e32 v94, s17
	v_mov_b32_e32 v95, s17
	v_mov_b32_e32 v96, s17
	v_mov_b32_e32 v97, s17
	v_mov_b32_e32 v98, s17
	v_mov_b32_e32 v99, s17
	v_mov_b32_e32 v100, s17
	v_mov_b32_e32 v101, s17
	v_mov_b32_e32 v102, s17
	v_mov_b32_e32 v103, s17
	v_mov_b32_e32 v104, s17
	v_mov_b32_e32 v105, s17
	v_mov_b32_e32 v120, s17
	v_cndmask_b32_e64 v91, v120, v91, s[14:15]
	v_cndmask_b32_e64 v92, v120, v92, s[14:15]
	v_cndmask_b32_e64 v93, v120, v93, s[14:15]
	v_max3_f32 v106, v106, v90, v91
	v_max3_f32 v106, v106, v92, v93
	v_max3_f32 v106, v106, v94, v95
	v_max3_f32 v106, v106, v96, v97
	v_max3_f32 v106, v106, v98, v99
	v_max3_f32 v106, v106, v100, v101
	v_max3_f32 v106, v106, v102, v103
	v_max3_f32 v106, v106, v104, v105
	v_mov_b32_e32 v120, v106
	v_mov_b32_e32 v121, v106
	s_nop 1
	v_permlane32_swap_b32_e32 v120, v121
	s_nop 1
	v_max3_f32 v106, v106, v120, v121
	v_mul_f32_e32 v106, s16, v106
	v_mov_b32_e32 v107, 0
	v_fma_f32 v120, v50, s16, -v106
	v_exp_f32_e32 v50, v120
	v_fma_f32 v121, v51, s16, -v106
	v_exp_f32_e32 v51, v121
	v_fma_f32 v122, v52, s16, -v106
	v_exp_f32_e32 v52, v122
	v_fma_f32 v123, v53, s16, -v106
	v_exp_f32_e32 v53, v123
	v_fma_f32 v120, v54, s16, -v106
	v_exp_f32_e32 v54, v120
	v_fma_f32 v121, v55, s16, -v106
	v_exp_f32_e32 v55, v121
	v_fma_f32 v122, v56, s16, -v106
	v_exp_f32_e32 v56, v122
	v_fma_f32 v123, v57, s16, -v106
	v_exp_f32_e32 v57, v123
	v_fma_f32 v120, v58, s16, -v106
	v_exp_f32_e32 v58, v120
	v_fma_f32 v121, v59, s16, -v106
	v_exp_f32_e32 v59, v121
	v_fma_f32 v122, v60, s16, -v106
	v_exp_f32_e32 v60, v122
	v_fma_f32 v123, v61, s16, -v106
	v_exp_f32_e32 v61, v123
	v_fma_f32 v120, v62, s16, -v106
	v_exp_f32_e32 v62, v120
	v_fma_f32 v121, v63, s16, -v106
	v_exp_f32_e32 v63, v121
	v_fma_f32 v122, v64, s16, -v106
	v_exp_f32_e32 v64, v122
	v_fma_f32 v123, v65, s16, -v106
	v_exp_f32_e32 v65, v123
	v_add_f32_e32 v107, v107, v50
	v_add_f32_e32 v107, v107, v51
	v_add_f32_e32 v107, v107, v52
	v_add_f32_e32 v107, v107, v53
	v_add_f32_e32 v107, v107, v54
	v_add_f32_e32 v107, v107, v55
	v_add_f32_e32 v107, v107, v56
	v_add_f32_e32 v107, v107, v57
	v_add_f32_e32 v107, v107, v58
	v_add_f32_e32 v107, v107, v59
	v_add_f32_e32 v107, v107, v60
	v_add_f32_e32 v107, v107, v61
	v_add_f32_e32 v107, v107, v62
	v_add_f32_e32 v107, v107, v63
	v_add_f32_e32 v107, v107, v64
	v_add_f32_e32 v107, v107, v65
	v_cvt_pk_f16_f32 v66, v50, v51
	v_cvt_pk_f16_f32 v67, v52, v53
	v_cvt_pk_f16_f32 v68, v54, v55
	v_cvt_pk_f16_f32 v69, v56, v57
	v_cvt_pk_f16_f32 v70, v58, v59
	v_cvt_pk_f16_f32 v71, v60, v61
	v_cvt_pk_f16_f32 v72, v62, v63
	v_cvt_pk_f16_f32 v73, v64, v65
	v_fma_f32 v120, v18, s16, -v106
	v_exp_f32_e32 v18, v120
	v_fma_f32 v121, v19, s16, -v106
	v_exp_f32_e32 v19, v121
	v_fma_f32 v122, v20, s16, -v106
	v_exp_f32_e32 v20, v122
	v_fma_f32 v123, v21, s16, -v106
	v_exp_f32_e32 v21, v123
	v_fma_f32 v120, v22, s16, -v106
	v_exp_f32_e32 v22, v120
	v_fma_f32 v121, v23, s16, -v106
	v_exp_f32_e32 v23, v121
	v_fma_f32 v122, v24, s16, -v106
	v_exp_f32_e32 v24, v122
	v_fma_f32 v123, v25, s16, -v106
	v_exp_f32_e32 v25, v123
	v_fma_f32 v120, v26, s16, -v106
	v_exp_f32_e32 v26, v120
	v_fma_f32 v121, v27, s16, -v106
	v_exp_f32_e32 v27, v121
	v_fma_f32 v122, v28, s16, -v106
	v_exp_f32_e32 v28, v122
	v_fma_f32 v123, v29, s16, -v106
	v_exp_f32_e32 v29, v123
	v_fma_f32 v120, v30, s16, -v106
	v_exp_f32_e32 v30, v120
	v_fma_f32 v121, v31, s16, -v106
	v_exp_f32_e32 v31, v121
	v_fma_f32 v122, v32, s16, -v106
	v_exp_f32_e32 v32, v122
	v_fma_f32 v123, v33, s16, -v106
	v_exp_f32_e32 v33, v123
	v_add_f32_e32 v107, v107, v18
	v_add_f32_e32 v107, v107, v19
	v_add_f32_e32 v107, v107, v20
	v_add_f32_e32 v107, v107, v21
	v_add_f32_e32 v107, v107, v22
	v_add_f32_e32 v107, v107, v23
	v_add_f32_e32 v107, v107, v24
	v_add_f32_e32 v107, v107, v25
	v_add_f32_e32 v107, v107, v26
	v_add_f32_e32 v107, v107, v27
	v_add_f32_e32 v107, v107, v28
	v_add_f32_e32 v107, v107, v29
	v_add_f32_e32 v107, v107, v30
	v_add_f32_e32 v107, v107, v31
	v_add_f32_e32 v107, v107, v32
	v_add_f32_e32 v107, v107, v33
	v_cvt_pk_f16_f32 v50, v18, v19
	v_cvt_pk_f16_f32 v51, v20, v21
	v_cvt_pk_f16_f32 v52, v22, v23
	v_cvt_pk_f16_f32 v53, v24, v25
	v_cvt_pk_f16_f32 v54, v26, v27
	v_cvt_pk_f16_f32 v55, v28, v29
	v_cvt_pk_f16_f32 v56, v30, v31
	v_cvt_pk_f16_f32 v57, v32, v33
	v_fma_f32 v120, v34, s16, -v106
	v_exp_f32_e32 v34, v120
	v_fma_f32 v121, v35, s16, -v106
	v_exp_f32_e32 v35, v121
	v_fma_f32 v122, v36, s16, -v106
	v_exp_f32_e32 v36, v122
	v_fma_f32 v123, v37, s16, -v106
	v_exp_f32_e32 v37, v123
	v_fma_f32 v120, v38, s16, -v106
	v_exp_f32_e32 v38, v120
	v_fma_f32 v121, v39, s16, -v106
	v_exp_f32_e32 v39, v121
	v_fma_f32 v122, v40, s16, -v106
	v_exp_f32_e32 v40, v122
	v_fma_f32 v123, v41, s16, -v106
	v_exp_f32_e32 v41, v123
	v_fma_f32 v120, v42, s16, -v106
	v_exp_f32_e32 v42, v120
	v_fma_f32 v121, v43, s16, -v106
	v_exp_f32_e32 v43, v121
	v_fma_f32 v122, v44, s16, -v106
	v_exp_f32_e32 v44, v122
	v_fma_f32 v123, v45, s16, -v106
	v_exp_f32_e32 v45, v123
	v_fma_f32 v120, v46, s16, -v106
	v_exp_f32_e32 v46, v120
	v_fma_f32 v121, v47, s16, -v106
	v_exp_f32_e32 v47, v121
	v_fma_f32 v122, v48, s16, -v106
	v_exp_f32_e32 v48, v122
	v_fma_f32 v123, v49, s16, -v106
	v_exp_f32_e32 v49, v123
	v_add_f32_e32 v107, v107, v34
	v_add_f32_e32 v107, v107, v35
	v_add_f32_e32 v107, v107, v36
	v_add_f32_e32 v107, v107, v37
	v_add_f32_e32 v107, v107, v38
	v_add_f32_e32 v107, v107, v39
	v_add_f32_e32 v107, v107, v40
	v_add_f32_e32 v107, v107, v41
	v_add_f32_e32 v107, v107, v42
	v_add_f32_e32 v107, v107, v43
	v_add_f32_e32 v107, v107, v44
	v_add_f32_e32 v107, v107, v45
	v_add_f32_e32 v107, v107, v46
	v_add_f32_e32 v107, v107, v47
	v_add_f32_e32 v107, v107, v48
	v_add_f32_e32 v107, v107, v49
	v_cvt_pk_f16_f32 v116, v34, v35
	v_cvt_pk_f16_f32 v117, v36, v37
	v_cvt_pk_f16_f32 v118, v38, v39
	v_cvt_pk_f16_f32 v119, v40, v41
	v_cvt_pk_f16_f32 v124, v42, v43
	v_cvt_pk_f16_f32 v125, v44, v45
	v_cvt_pk_f16_f32 v126, v46, v47
	v_cvt_pk_f16_f32 v127, v48, v49
	v_mov_b32_e32 v18, 0
	v_mov_b32_e32 v19, 0
	v_mov_b32_e32 v20, 0
	v_mov_b32_e32 v21, 0
	v_mov_b32_e32 v22, 0
	v_mov_b32_e32 v23, 0
	v_mov_b32_e32 v24, 0
	v_mov_b32_e32 v25, 0
	v_mov_b32_e32 v26, 0
	v_mov_b32_e32 v27, 0
	v_mov_b32_e32 v28, 0
	v_mov_b32_e32 v29, 0
	v_mov_b32_e32 v30, 0
	v_mov_b32_e32 v31, 0
	v_mov_b32_e32 v32, 0
	v_mov_b32_e32 v33, 0
	v_mov_b32_e32 v34, 0
	v_mov_b32_e32 v35, 0
	v_mov_b32_e32 v36, 0
	v_mov_b32_e32 v37, 0
	v_mov_b32_e32 v38, 0
	v_mov_b32_e32 v39, 0
	v_mov_b32_e32 v40, 0
	v_mov_b32_e32 v41, 0
	v_mov_b32_e32 v42, 0
	v_mov_b32_e32 v43, 0
	v_mov_b32_e32 v44, 0
	v_mov_b32_e32 v45, 0
	v_mov_b32_e32 v46, 0
	v_mov_b32_e32 v47, 0
	v_mov_b32_e32 v48, 0
	v_mov_b32_e32 v49, 0
	ds_read2_b64 v[58:61], v113 offset0:24 offset1:26
	ds_read2_b64 v[62:65], v114 offset0:24 offset1:26
	s_nop 1
	s_waitcnt lgkmcnt(1)
	v_mfma_f32_32x32x16_f16 v[18:33], v[58:61], v[66:69], v[18:33]
	ds_read2_b64 v[58:61], v113 offset0:28 offset1:30
	s_waitcnt lgkmcnt(1)
	v_mfma_f32_32x32x16_f16 v[34:49], v[62:65], v[66:69], v[34:49]
	ds_read2_b64 v[62:65], v114 offset0:28 offset1:30
	s_waitcnt lgkmcnt(1)
	v_mfma_f32_32x32x16_f16 v[18:33], v[58:61], v[70:73], v[18:33]
	s_waitcnt lgkmcnt(0)
	v_mfma_f32_32x32x16_f16 v[34:49], v[62:65], v[70:73], v[34:49]
	ds_read2_b64 v[58:61], v113 offset0:32 offset1:34
	ds_read2_b64 v[62:65], v114 offset0:32 offset1:34
	s_nop 1
	s_waitcnt lgkmcnt(1)
	v_mfma_f32_32x32x16_f16 v[18:33], v[58:61], v[50:53], v[18:33]
	ds_read2_b64 v[58:61], v113 offset0:36 offset1:38
	s_waitcnt lgkmcnt(1)
	v_mfma_f32_32x32x16_f16 v[34:49], v[62:65], v[50:53], v[34:49]
	ds_read2_b64 v[62:65], v114 offset0:36 offset1:38
	s_waitcnt lgkmcnt(1)
	v_mfma_f32_32x32x16_f16 v[18:33], v[58:61], v[54:57], v[18:33]
	s_waitcnt lgkmcnt(0)
	v_mfma_f32_32x32x16_f16 v[34:49], v[62:65], v[54:57], v[34:49]
	ds_read2_b64 v[58:61], v113 offset0:40 offset1:42
	ds_read2_b64 v[62:65], v114 offset0:40 offset1:42
	s_nop 1
	s_waitcnt lgkmcnt(1)
	v_mfma_f32_32x32x16_f16 v[18:33], v[58:61], v[116:119], v[18:33]
	ds_read2_b64 v[58:61], v113 offset0:44 offset1:46
	s_waitcnt lgkmcnt(1)
	v_mfma_f32_32x32x16_f16 v[34:49], v[62:65], v[116:119], v[34:49]
	ds_read2_b64 v[62:65], v114 offset0:44 offset1:46
	s_waitcnt lgkmcnt(1)
	v_mfma_f32_32x32x16_f16 v[18:33], v[58:61], v[124:127], v[18:33]
	s_waitcnt lgkmcnt(0)
	v_mfma_f32_32x32x16_f16 v[34:49], v[62:65], v[124:127], v[34:49]
	v_fma_f32 v120, v90, s16, -v106
	v_exp_f32_e32 v90, v120
	v_fma_f32 v121, v91, s16, -v106
	v_exp_f32_e32 v91, v121
	v_fma_f32 v122, v92, s16, -v106
	v_exp_f32_e32 v92, v122
	v_fma_f32 v123, v93, s16, -v106
	v_exp_f32_e32 v93, v123
	v_fma_f32 v120, v94, s16, -v106
	v_exp_f32_e32 v94, v120
	v_fma_f32 v121, v95, s16, -v106
	v_exp_f32_e32 v95, v121
	v_fma_f32 v122, v96, s16, -v106
	v_exp_f32_e32 v96, v122
	v_fma_f32 v123, v97, s16, -v106
	v_exp_f32_e32 v97, v123
	v_fma_f32 v120, v98, s16, -v106
	v_exp_f32_e32 v98, v120
	v_fma_f32 v121, v99, s16, -v106
	v_exp_f32_e32 v99, v121
	v_fma_f32 v122, v100, s16, -v106
	v_exp_f32_e32 v100, v122
	v_fma_f32 v123, v101, s16, -v106
	v_exp_f32_e32 v101, v123
	v_fma_f32 v120, v102, s16, -v106
	v_exp_f32_e32 v102, v120
	v_fma_f32 v121, v103, s16, -v106
	v_exp_f32_e32 v103, v121
	v_fma_f32 v122, v104, s16, -v106
	v_exp_f32_e32 v104, v122
	v_fma_f32 v123, v105, s16, -v106
	v_exp_f32_e32 v105, v123
	v_add_f32_e32 v107, v107, v90
	v_add_f32_e32 v107, v107, v91
	v_add_f32_e32 v107, v107, v92
	v_add_f32_e32 v107, v107, v93
	v_add_f32_e32 v107, v107, v94
	v_add_f32_e32 v107, v107, v95
	v_add_f32_e32 v107, v107, v96
	v_add_f32_e32 v107, v107, v97
	v_add_f32_e32 v107, v107, v98
	v_add_f32_e32 v107, v107, v99
	v_add_f32_e32 v107, v107, v100
	v_add_f32_e32 v107, v107, v101
	v_add_f32_e32 v107, v107, v102
	v_add_f32_e32 v107, v107, v103
	v_add_f32_e32 v107, v107, v104
	v_add_f32_e32 v107, v107, v105
	v_cvt_pk_f16_f32 v50, v90, v91
	v_cvt_pk_f16_f32 v51, v92, v93
	v_cvt_pk_f16_f32 v52, v94, v95
	v_cvt_pk_f16_f32 v53, v96, v97
	v_cvt_pk_f16_f32 v54, v98, v99
	v_cvt_pk_f16_f32 v55, v100, v101
	v_cvt_pk_f16_f32 v56, v102, v103
	v_cvt_pk_f16_f32 v57, v104, v105
	ds_read2_b64 v[58:61], v113 offset0:48 offset1:50
	ds_read2_b64 v[62:65], v114 offset0:48 offset1:50
	s_nop 1
	s_waitcnt lgkmcnt(1)
	v_mfma_f32_32x32x16_f16 v[18:33], v[58:61], v[50:53], v[18:33]
	ds_read2_b64 v[58:61], v113 offset0:52 offset1:54
	s_waitcnt lgkmcnt(1)
	v_mfma_f32_32x32x16_f16 v[34:49], v[62:65], v[50:53], v[34:49]
	ds_read2_b64 v[62:65], v114 offset0:52 offset1:54
	s_waitcnt lgkmcnt(1)
	v_mfma_f32_32x32x16_f16 v[18:33], v[58:61], v[54:57], v[18:33]
	s_waitcnt lgkmcnt(0)
	v_mfma_f32_32x32x16_f16 v[34:49], v[62:65], v[54:57], v[34:49]
	ds_read_b128 v[66:69], v112 offset:0
	ds_read_b128 v[70:73], v112 offset:32
	s_waitcnt lgkmcnt(1)
	v_mfma_f32_32x32x16_f16 v[90:105], v[66:69], v[74:77], 0
	v_fma_f32 v120, v2, s16, -v106
	v_exp_f32_e32 v2, v120
	v_fma_f32 v121, v3, s16, -v106
	v_exp_f32_e32 v3, v121
	v_fma_f32 v122, v4, s16, -v106
	v_exp_f32_e32 v4, v122
	v_fma_f32 v123, v5, s16, -v106
	v_exp_f32_e32 v5, v123
	v_fma_f32 v120, v6, s16, -v106
	v_exp_f32_e32 v6, v120
	v_fma_f32 v121, v7, s16, -v106
	v_exp_f32_e32 v7, v121
	ds_read_b128 v[66:69], v112 offset:64
	s_waitcnt lgkmcnt(1)
	v_mfma_f32_32x32x16_f16 v[90:105], v[70:73], v[78:81], v[90:105]
	v_fma_f32 v122, v8, s16, -v106
	v_exp_f32_e32 v8, v122
	v_fma_f32 v123, v9, s16, -v106
	v_exp_f32_e32 v9, v123
	v_fma_f32 v120, v10, s16, -v106
	v_exp_f32_e32 v10, v120
	v_fma_f32 v121, v11, s16, -v106
	v_exp_f32_e32 v11, v121
	v_fma_f32 v122, v12, s16, -v106
	v_exp_f32_e32 v12, v122
	v_fma_f32 v123, v13, s16, -v106
	v_exp_f32_e32 v13, v123
	ds_read_b128 v[70:73], v112 offset:96
	s_waitcnt lgkmcnt(1)
	v_mfma_f32_32x32x16_f16 v[90:105], v[66:69], v[82:85], v[90:105]
	v_fma_f32 v120, v14, s16, -v106
	v_exp_f32_e32 v14, v120
	v_fma_f32 v121, v15, s16, -v106
	v_exp_f32_e32 v15, v121
	v_fma_f32 v122, v16, s16, -v106
	v_exp_f32_e32 v16, v122
	v_fma_f32 v123, v17, s16, -v106
	v_exp_f32_e32 v17, v123
	v_add_f32_e32 v107, v107, v2
	v_add_f32_e32 v107, v107, v3
	v_add_f32_e32 v107, v107, v4
	v_add_f32_e32 v107, v107, v5
	s_waitcnt lgkmcnt(0)
	v_mfma_f32_32x32x16_f16 v[90:105], v[70:73], v[86:89], v[90:105]
	v_add_f32_e32 v107, v107, v6
	v_add_f32_e32 v107, v107, v7
	v_add_f32_e32 v107, v107, v8
	v_add_f32_e32 v107, v107, v9
	v_add_f32_e32 v107, v107, v10
	v_add_f32_e32 v107, v107, v11
	v_add_f32_e32 v107, v107, v12
	v_add_f32_e32 v107, v107, v13
	v_add_f32_e32 v107, v107, v14
	v_add_f32_e32 v107, v107, v15
	v_add_f32_e32 v107, v107, v16
	v_add_f32_e32 v107, v107, v17
	v_cvt_pk_f16_f32 v50, v2, v3
	v_cvt_pk_f16_f32 v51, v4, v5
	v_cvt_pk_f16_f32 v52, v6, v7
	v_cvt_pk_f16_f32 v53, v8, v9
	v_cvt_pk_f16_f32 v54, v10, v11
	v_cvt_pk_f16_f32 v55, v12, v13
	v_cvt_pk_f16_f32 v56, v14, v15
	v_cvt_pk_f16_f32 v57, v16, v17
	ds_read2_b64 v[58:61], v113 offset0:16 offset1:18
	ds_read2_b64 v[62:65], v114 offset0:16 offset1:18
	s_nop 1
	s_waitcnt lgkmcnt(1)
	v_mfma_f32_32x32x16_f16 v[18:33], v[58:61], v[50:53], v[18:33]
	ds_read2_b64 v[58:61], v113 offset0:20 offset1:22
	s_waitcnt lgkmcnt(1)
	v_mfma_f32_32x32x16_f16 v[34:49], v[62:65], v[50:53], v[34:49]
	ds_read2_b64 v[62:65], v114 offset0:20 offset1:22
	s_waitcnt lgkmcnt(1)
	v_mfma_f32_32x32x16_f16 v[18:33], v[58:61], v[54:57], v[18:33]
	s_waitcnt lgkmcnt(0)
	v_mfma_f32_32x32x16_f16 v[34:49], v[62:65], v[54:57], v[34:49]
	ds_read_b128 v[66:69], v112 offset:4608
	ds_read_b128 v[70:73], v112 offset:4640
	s_waitcnt lgkmcnt(1)
	v_mfma_f32_32x32x16_f16 v[2:17], v[66:69], v[74:77], 0
	v_fma_f32 v120, v90, s16, -v106
	v_exp_f32_e32 v90, v120
	v_fma_f32 v121, v91, s16, -v106
	v_exp_f32_e32 v91, v121
	v_fma_f32 v122, v92, s16, -v106
	v_exp_f32_e32 v92, v122
	v_fma_f32 v123, v93, s16, -v106
	v_exp_f32_e32 v93, v123
	v_fma_f32 v120, v94, s16, -v106
	v_exp_f32_e32 v94, v120
	v_fma_f32 v121, v95, s16, -v106
	v_exp_f32_e32 v95, v121
	ds_read_b128 v[66:69], v112 offset:4672
	s_waitcnt lgkmcnt(1)
	v_mfma_f32_32x32x16_f16 v[2:17], v[70:73], v[78:81], v[2:17]
	v_fma_f32 v122, v96, s16, -v106
	v_exp_f32_e32 v96, v122
	v_fma_f32 v123, v97, s16, -v106
	v_exp_f32_e32 v97, v123
	v_fma_f32 v120, v98, s16, -v106
	v_exp_f32_e32 v98, v120
	v_fma_f32 v121, v99, s16, -v106
	v_exp_f32_e32 v99, v121
	v_fma_f32 v122, v100, s16, -v106
	v_exp_f32_e32 v100, v122
	v_fma_f32 v123, v101, s16, -v106
	v_exp_f32_e32 v101, v123
	ds_read_b128 v[70:73], v112 offset:4704
	s_waitcnt lgkmcnt(1)
	v_mfma_f32_32x32x16_f16 v[2:17], v[66:69], v[82:85], v[2:17]
	v_fma_f32 v120, v102, s16, -v106
	v_exp_f32_e32 v102, v120
	v_fma_f32 v121, v103, s16, -v106
	v_exp_f32_e32 v103, v121
	v_fma_f32 v122, v104, s16, -v106
	v_exp_f32_e32 v104, v122
	v_fma_f32 v123, v105, s16, -v106
	v_exp_f32_e32 v105, v123
	v_add_f32_e32 v107, v107, v90
	v_add_f32_e32 v107, v107, v91
	v_add_f32_e32 v107, v107, v92
	v_add_f32_e32 v107, v107, v93
	s_waitcnt lgkmcnt(0)
	v_mfma_f32_32x32x16_f16 v[2:17], v[70:73], v[86:89], v[2:17]
	v_add_f32_e32 v107, v107, v94
	v_add_f32_e32 v107, v107, v95
	v_add_f32_e32 v107, v107, v96
	v_add_f32_e32 v107, v107, v97
	v_add_f32_e32 v107, v107, v98
	v_add_f32_e32 v107, v107, v99
	v_add_f32_e32 v107, v107, v100
	v_add_f32_e32 v107, v107, v101
	v_add_f32_e32 v107, v107, v102
	v_add_f32_e32 v107, v107, v103
	v_add_f32_e32 v107, v107, v104
	v_add_f32_e32 v107, v107, v105
	v_cvt_pk_f16_f32 v50, v90, v91
	v_cvt_pk_f16_f32 v51, v92, v93
	v_cvt_pk_f16_f32 v52, v94, v95
	v_cvt_pk_f16_f32 v53, v96, v97
	v_cvt_pk_f16_f32 v54, v98, v99
	v_cvt_pk_f16_f32 v55, v100, v101
	v_cvt_pk_f16_f32 v56, v102, v103
	v_cvt_pk_f16_f32 v57, v104, v105
	ds_read2_b64 v[58:61], v113 offset0:0 offset1:2
	ds_read2_b64 v[62:65], v114 offset0:0 offset1:2
	s_nop 1
	s_waitcnt lgkmcnt(1)
	v_mfma_f32_32x32x16_f16 v[18:33], v[58:61], v[50:53], v[18:33]
	ds_read2_b64 v[58:61], v113 offset0:4 offset1:6
	s_waitcnt lgkmcnt(1)
	v_mfma_f32_32x32x16_f16 v[34:49], v[62:65], v[50:53], v[34:49]
	ds_read2_b64 v[62:65], v114 offset0:4 offset1:6
	s_waitcnt lgkmcnt(1)
	v_mfma_f32_32x32x16_f16 v[18:33], v[58:61], v[54:57], v[18:33]
	s_waitcnt lgkmcnt(0)
	v_mfma_f32_32x32x16_f16 v[34:49], v[62:65], v[54:57], v[34:49]
	s_nop 15
	s_nop 1
	v_fma_f32 v120, v2, s16, -v106
	v_exp_f32_e32 v2, v120
	v_fma_f32 v121, v3, s16, -v106
	v_exp_f32_e32 v3, v121
	v_fma_f32 v122, v4, s16, -v106
	v_exp_f32_e32 v4, v122
	v_fma_f32 v123, v5, s16, -v106
	v_exp_f32_e32 v5, v123
	v_fma_f32 v120, v6, s16, -v106
	v_exp_f32_e32 v6, v120
	v_fma_f32 v121, v7, s16, -v106
	v_exp_f32_e32 v7, v121
	v_fma_f32 v122, v8, s16, -v106
	v_exp_f32_e32 v8, v122
	v_fma_f32 v123, v9, s16, -v106
	v_exp_f32_e32 v9, v123
	v_fma_f32 v120, v10, s16, -v106
	v_exp_f32_e32 v10, v120
	v_fma_f32 v121, v11, s16, -v106
	v_exp_f32_e32 v11, v121
	v_fma_f32 v122, v12, s16, -v106
	v_exp_f32_e32 v12, v122
	v_fma_f32 v123, v13, s16, -v106
	v_exp_f32_e32 v13, v123
	v_fma_f32 v120, v14, s16, -v106
	v_exp_f32_e32 v14, v120
	v_fma_f32 v121, v15, s16, -v106
	v_exp_f32_e32 v15, v121
	v_fma_f32 v122, v16, s16, -v106
	v_exp_f32_e32 v16, v122
	v_fma_f32 v123, v17, s16, -v106
	v_exp_f32_e32 v17, v123
	v_add_f32_e32 v107, v107, v2
	v_add_f32_e32 v107, v107, v3
	v_add_f32_e32 v107, v107, v4
	v_add_f32_e32 v107, v107, v5
	v_add_f32_e32 v107, v107, v6
	v_add_f32_e32 v107, v107, v7
	v_add_f32_e32 v107, v107, v8
	v_add_f32_e32 v107, v107, v9
	v_add_f32_e32 v107, v107, v10
	v_add_f32_e32 v107, v107, v11
	v_add_f32_e32 v107, v107, v12
	v_add_f32_e32 v107, v107, v13
	v_add_f32_e32 v107, v107, v14
	v_add_f32_e32 v107, v107, v15
	v_add_f32_e32 v107, v107, v16
	v_add_f32_e32 v107, v107, v17
	v_cvt_pk_f16_f32 v50, v2, v3
	v_cvt_pk_f16_f32 v51, v4, v5
	v_cvt_pk_f16_f32 v52, v6, v7
	v_cvt_pk_f16_f32 v53, v8, v9
	v_cvt_pk_f16_f32 v54, v10, v11
	v_cvt_pk_f16_f32 v55, v12, v13
	v_cvt_pk_f16_f32 v56, v14, v15
	v_cvt_pk_f16_f32 v57, v16, v17
	ds_read2_b64 v[58:61], v113 offset0:8 offset1:10
	ds_read2_b64 v[62:65], v114 offset0:8 offset1:10
	s_nop 1
	s_waitcnt lgkmcnt(1)
	v_mfma_f32_32x32x16_f16 v[18:33], v[58:61], v[50:53], v[18:33]
	ds_read2_b64 v[58:61], v113 offset0:12 offset1:14
	s_waitcnt lgkmcnt(1)
	v_mfma_f32_32x32x16_f16 v[34:49], v[62:65], v[50:53], v[34:49]
	ds_read2_b64 v[62:65], v114 offset0:12 offset1:14
	s_waitcnt lgkmcnt(1)
	v_mfma_f32_32x32x16_f16 v[18:33], v[58:61], v[54:57], v[18:33]
	s_waitcnt lgkmcnt(0)
	v_mfma_f32_32x32x16_f16 v[34:49], v[62:65], v[54:57], v[34:49]
	v_mov_b32_e32 v120, v107
	v_mov_b32_e32 v121, v107
	s_nop 1
	v_permlane32_swap_b32_e32 v120, v121
	s_nop 1
	v_add_f32_e32 v107, v120, v121
	v_log_f32_e32 v122, v107
	v_rcp_f32_e32 v123, v107
	s_nop 0
	v_add_f32_e32 v122, v122, v106
	v_fma_f32 v124, -v107, v123, 2.0
	v_mul_f32_e32 v123, v123, v124
	v_lshlrev_b32_e32 v125, 2, v109
	s_mov_b64 s[18:19], exec
	s_and_b64 exec, exec, s[14:15]
	ds_write_b32 v125, v122 offset:61440
	s_mov_b64 exec, s[18:19]
	s_mul_i32 s20, s2, 0x493
	s_lshr_b32 s20, s20, 16
	s_mul_i32 s21, s20, 56
	s_sub_u32 s21, s2, s21
	s_mul_i32 s22, s21, 0x2493
	s_lshr_b32 s22, s22, 16
	s_mul_i32 s23, s22, 7
	s_sub_u32 s23, s21, s23
	s_mul_i32 s24, s23, 0xc5
	s_lshl_b32 s24, s24, 13
	s_lshl_b32 s25, s22, 10
	s_add_u32 s24, s24, s25
	s_lshl_b32 s25, s20, 7
	s_add_u32 s24, s24, s25
	v_lshlrev_b32_e32 v125, 13, v110
	v_add3_u32 v125, v125, s24, v111
	s_nop 15
	s_waitcnt lgkmcnt(0)
	v_mul_f32_e32 v18, v18, v123
	v_mul_f32_e32 v19, v19, v123
	v_mul_f32_e32 v20, v20, v123
	v_mul_f32_e32 v21, v21, v123
	v_mul_f32_e32 v22, v22, v123
	v_mul_f32_e32 v23, v23, v123
	v_mul_f32_e32 v24, v24, v123
	v_mul_f32_e32 v25, v25, v123
	v_cvt_pk_f16_f32 v50, v18, v19
	v_cvt_pk_f16_f32 v51, v20, v21
	v_cvt_pk_f16_f32 v52, v22, v23
	v_cvt_pk_f16_f32 v53, v24, v25
	s_nop 1
	v_permlane32_swap_b32_e32 v50, v52
	v_permlane32_swap_b32_e32 v51, v53
	s_nop 1
	s_and_b64 exec, exec, s[12:13]
	global_store_dwordx4 v125, v[50:53], s[8:9] offset:0
	s_mov_b64 exec, s[18:19]
	s_nop 1
	v_mul_f32_e32 v26, v26, v123
	v_mul_f32_e32 v27, v27, v123
	v_mul_f32_e32 v28, v28, v123
	v_mul_f32_e32 v29, v29, v123
	v_mul_f32_e32 v30, v30, v123
	v_mul_f32_e32 v31, v31, v123
	v_mul_f32_e32 v32, v32, v123
	v_mul_f32_e32 v33, v33, v123
	v_cvt_pk_f16_f32 v54, v26, v27
	v_cvt_pk_f16_f32 v55, v28, v29
	v_cvt_pk_f16_f32 v56, v30, v31
	v_cvt_pk_f16_f32 v57, v32, v33
	s_nop 1
	v_permlane32_swap_b32_e32 v54, v56
	v_permlane32_swap_b32_e32 v55, v57
	s_nop 1
	s_and_b64 exec, exec, s[12:13]
	global_store_dwordx4 v125, v[54:57], s[8:9] offset:32
	s_mov_b64 exec, s[18:19]
	s_nop 1
	v_mul_f32_e32 v34, v34, v123
	v_mul_f32_e32 v35, v35, v123
	v_mul_f32_e32 v36, v36, v123
	v_mul_f32_e32 v37, v37, v123
	v_mul_f32_e32 v38, v38, v123
	v_mul_f32_e32 v39, v39, v123
	v_mul_f32_e32 v40, v40, v123
	v_mul_f32_e32 v41, v41, v123
	v_cvt_pk_f16_f32 v50, v34, v35
	v_cvt_pk_f16_f32 v51, v36, v37
	v_cvt_pk_f16_f32 v52, v38, v39
	v_cvt_pk_f16_f32 v53, v40, v41
	s_nop 1
	v_permlane32_swap_b32_e32 v50, v52
	v_permlane32_swap_b32_e32 v51, v53
	s_nop 1
	s_and_b64 exec, exec, s[12:13]
	global_store_dwordx4 v125, v[50:53], s[8:9] offset:64
	s_mov_b64 exec, s[18:19]
	s_nop 1
	v_mul_f32_e32 v42, v42, v123
	v_mul_f32_e32 v43, v43, v123
	v_mul_f32_e32 v44, v44, v123
	v_mul_f32_e32 v45, v45, v123
	v_mul_f32_e32 v46, v46, v123
	v_mul_f32_e32 v47, v47, v123
	v_mul_f32_e32 v48, v48, v123
	v_mul_f32_e32 v49, v49, v123
	v_cvt_pk_f16_f32 v54, v42, v43
	v_cvt_pk_f16_f32 v55, v44, v45
	v_cvt_pk_f16_f32 v56, v46, v47
	v_cvt_pk_f16_f32 v57, v48, v49
	s_nop 1
	v_permlane32_swap_b32_e32 v54, v56
	v_permlane32_swap_b32_e32 v55, v57
	s_nop 1
	s_and_b64 exec, exec, s[12:13]
	global_store_dwordx4 v125, v[54:57], s[8:9] offset:96
	s_mov_b64 exec, s[18:19]
	s_nop 1
	s_waitcnt lgkmcnt(0)
	s_barrier
	v_lshl_add_u32 v120, v115, 2, v111
	ds_read_b128 v[90:93], v120 offset:61440
	ds_read_b128 v[94:97], v120 offset:61472
	ds_read_b128 v[98:101], v120 offset:61504
	ds_read_b128 v[102:105], v120 offset:61536
	v_lshl_or_b32 v121, v1, 2, v115
	v_mul_u32_u24_e32 v121, 0xc5, v121
	v_add_lshl_u32 v116, v121, v108, 2
	v_add_u32_e32 v117, 0x18a0, v116
	v_add_u32_e32 v118, 0x3140, v116
	v_add_u32_e32 v119, 0x49e0, v116
	s_mul_hi_u32 s21, s2, 0x25e64
	s_mul_i32 s20, s2, 0x25e64
	s_add_u32 s10, s10, s20
	s_addc_u32 s11, s11, s21
	v_cmp_gt_u32_e64 s[22:23], 5, v108
	s_nop 0
	v_readfirstlane_b32 s26, v115
	s_cmp_eq_u32 s26, 0xc0
	s_cbranch_scc1 .Lsp_wave6
	ds_read_b128 v[66:69], v112 offset:0
	ds_read_b128 v[70:73], v112 offset:32
	s_waitcnt lgkmcnt(1)
	v_mfma_f32_32x32x16_f16 v[2:17], v[74:77], v[66:69], 0
	ds_read_b128 v[66:69], v112 offset:64
	s_waitcnt lgkmcnt(1)
	v_mfma_f32_32x32x16_f16 v[2:17], v[78:81], v[70:73], v[2:17]
	ds_read_b128 v[70:73], v112 offset:96
	s_waitcnt lgkmcnt(1)
	v_mfma_f32_32x32x16_f16 v[2:17], v[82:85], v[66:69], v[2:17]
	s_waitcnt lgkmcnt(0)
	v_mfma_f32_32x32x16_f16 v[2:17], v[86:89], v[70:73], v[2:17]
	s_waitcnt lgkmcnt(0)
	ds_read_b128 v[66:69], v112 offset:4608
	ds_read_b128 v[70:73], v112 offset:4640
	s_waitcnt lgkmcnt(1)
	v_mfma_f32_32x32x16_f16 v[18:33], v[74:77], v[66:69], 0
	ds_read_b128 v[66:69], v112 offset:4672
	s_waitcnt lgkmcnt(1)
	v_mfma_f32_32x32x16_f16 v[18:33], v[78:81], v[70:73], v[18:33]
	ds_read_b128 v[70:73], v112 offset:4704
	s_waitcnt lgkmcnt(1)
	v_mfma_f32_32x32x16_f16 v[18:33], v[82:85], v[66:69], v[18:33]
	s_waitcnt lgkmcnt(0)
	v_mfma_f32_32x32x16_f16 v[18:33], v[86:89], v[70:73], v[18:33]
	v_fma_f32 v120, v2, s16, -v90
	v_exp_f32_e32 v2, v120
	v_fma_f32 v121, v3, s16, -v91
	v_exp_f32_e32 v3, v121
	v_fma_f32 v122, v4, s16, -v92
	v_exp_f32_e32 v4, v122
	v_fma_f32 v123, v5, s16, -v93
	v_exp_f32_e32 v5, v123
	v_fma_f32 v120, v6, s16, -v94
	v_exp_f32_e32 v6, v120
	v_fma_f32 v121, v7, s16, -v95
	v_exp_f32_e32 v7, v121
	v_fma_f32 v122, v8, s16, -v96
	v_exp_f32_e32 v8, v122
	v_fma_f32 v123, v9, s16, -v97
	v_exp_f32_e32 v9, v123
	v_fma_f32 v120, v10, s16, -v98
	v_exp_f32_e32 v10, v120
	v_fma_f32 v121, v11, s16, -v99
	v_exp_f32_e32 v11, v121
	v_fma_f32 v122, v12, s16, -v100
	v_exp_f32_e32 v12, v122
	v_fma_f32 v123, v13, s16, -v101
	v_exp_f32_e32 v13, v123
	v_fma_f32 v120, v14, s16, -v102
	v_exp_f32_e32 v14, v120
	v_fma_f32 v121, v15, s16, -v103
	v_exp_f32_e32 v15, v121
	v_fma_f32 v122, v16, s16, -v104
	v_exp_f32_e32 v16, v122
	v_fma_f32 v123, v17, s16, -v105
	v_exp_f32_e32 v17, v123
	global_store_dword v116, v2, s[10:11] offset:0
	global_store_dword v116, v3, s[10:11] offset:788
	global_store_dword v116, v4, s[10:11] offset:1576
	global_store_dword v116, v5, s[10:11] offset:2364
	global_store_dword v117, v6, s[10:11] offset:0
	global_store_dword v117, v7, s[10:11] offset:788
	global_store_dword v117, v8, s[10:11] offset:1576
	global_store_dword v117, v9, s[10:11] offset:2364
	global_store_dword v118, v10, s[10:11] offset:0
	global_store_dword v118, v11, s[10:11] offset:788
	global_store_dword v118, v12, s[10:11] offset:1576
	global_store_dword v118, v13, s[10:11] offset:2364
	global_store_dword v119, v14, s[10:11] offset:0
	global_store_dword v119, v15, s[10:11] offset:788
	global_store_dword v119, v16, s[10:11] offset:1576
	global_store_dword v119, v17, s[10:11] offset:2364
	ds_read_b128 v[66:69], v112 offset:9216
	ds_read_b128 v[70:73], v112 offset:9248
	s_waitcnt lgkmcnt(1)
	v_mfma_f32_32x32x16_f16 v[2:17], v[74:77], v[66:69], 0
	v_fma_f32 v120, v18, s16, -v90
	v_exp_f32_e32 v18, v120
	v_fma_f32 v121, v19, s16, -v91
	v_exp_f32_e32 v19, v121
	v_fma_f32 v122, v20, s16, -v92
	v_exp_f32_e32 v20, v122
	v_fma_f32 v123, v21, s16, -v93
	v_exp_f32_e32 v21, v123
	v_fma_f32 v120, v22, s16, -v94
	v_exp_f32_e32 v22, v120
	v_fma_f32 v121, v23, s16, -v95
	v_exp_f32_e32 v23, v121
	ds_read_b128 v[66:69], v112 offset:9280
	s_waitcnt lgkmcnt(1)
	v_mfma_f32_32x32x16_f16 v[2:17], v[78:81], v[70:73], v[2:17]
	v_fma_f32 v122, v24, s16, -v96
	v_exp_f32_e32 v24, v122
	v_fma_f32 v123, v25, s16, -v97
	v_exp_f32_e32 v25, v123
	v_fma_f32 v120, v26, s16, -v98
	v_exp_f32_e32 v26, v120
	v_fma_f32 v121, v27, s16, -v99
	v_exp_f32_e32 v27, v121
	v_fma_f32 v122, v28, s16, -v100
	v_exp_f32_e32 v28, v122
	v_fma_f32 v123, v29, s16, -v101
	v_exp_f32_e32 v29, v123
	ds_read_b128 v[70:73], v112 offset:9312
	s_waitcnt lgkmcnt(1)
	v_mfma_f32_32x32x16_f16 v[2:17], v[82:85], v[66:69], v[2:17]
	v_fma_f32 v120, v30, s16, -v102
	v_exp_f32_e32 v30, v120
	v_fma_f32 v121, v31, s16, -v103
	v_exp_f32_e32 v31, v121
	v_fma_f32 v122, v32, s16, -v104
	v_exp_f32_e32 v32, v122
	v_fma_f32 v123, v33, s16, -v105
	v_exp_f32_e32 v33, v123
	global_store_dword v116, v18, s[10:11] offset:128
	global_store_dword v116, v19, s[10:11] offset:916
	global_store_dword v116, v20, s[10:11] offset:1704
	global_store_dword v116, v21, s[10:11] offset:2492
	s_waitcnt lgkmcnt(0)
	v_mfma_f32_32x32x16_f16 v[2:17], v[86:89], v[70:73], v[2:17]
	global_store_dword v117, v22, s[10:11] offset:128
	global_store_dword v117, v23, s[10:11] offset:916
	global_store_dword v117, v24, s[10:11] offset:1704
	global_store_dword v117, v25, s[10:11] offset:2492
	global_store_dword v118, v26, s[10:11] offset:128
	global_store_dword v118, v27, s[10:11] offset:916
	global_store_dword v118, v28, s[10:11] offset:1704
	global_store_dword v118, v29, s[10:11] offset:2492
	global_store_dword v119, v30, s[10:11] offset:128
	global_store_dword v119, v31, s[10:11] offset:916
	global_store_dword v119, v32, s[10:11] offset:1704
	global_store_dword v119, v33, s[10:11] offset:2492
	ds_read_b128 v[66:69], v112 offset:13824
	ds_read_b128 v[70:73], v112 offset:13856
	s_waitcnt lgkmcnt(1)
	v_mfma_f32_32x32x16_f16 v[18:33], v[74:77], v[66:69], 0
	v_fma_f32 v120, v2, s16, -v90
	v_exp_f32_e32 v2, v120
	v_fma_f32 v121, v3, s16, -v91
	v_exp_f32_e32 v3, v121
	v_fma_f32 v122, v4, s16, -v92
	v_exp_f32_e32 v4, v122
	v_fma_f32 v123, v5, s16, -v93
	v_exp_f32_e32 v5, v123
	v_fma_f32 v120, v6, s16, -v94
	v_exp_f32_e32 v6, v120
	v_fma_f32 v121, v7, s16, -v95
	v_exp_f32_e32 v7, v121
	ds_read_b128 v[66:69], v112 offset:13888
	s_waitcnt lgkmcnt(1)
	v_mfma_f32_32x32x16_f16 v[18:33], v[78:81], v[70:73], v[18:33]
	v_fma_f32 v122, v8, s16, -v96
	v_exp_f32_e32 v8, v122
	v_fma_f32 v123, v9, s16, -v97
	v_exp_f32_e32 v9, v123
	v_fma_f32 v120, v10, s16, -v98
	v_exp_f32_e32 v10, v120
	v_fma_f32 v121, v11, s16, -v99
	v_exp_f32_e32 v11, v121
	v_fma_f32 v122, v12, s16, -v100
	v_exp_f32_e32 v12, v122
	v_fma_f32 v123, v13, s16, -v101
	v_exp_f32_e32 v13, v123
	ds_read_b128 v[70:73], v112 offset:13920
	s_waitcnt lgkmcnt(1)
	v_mfma_f32_32x32x16_f16 v[18:33], v[82:85], v[66:69], v[18:33]
	v_fma_f32 v120, v14, s16, -v102
	v_exp_f32_e32 v14, v120
	v_fma_f32 v121, v15, s16, -v103
	v_exp_f32_e32 v15, v121
	v_fma_f32 v122, v16, s16, -v104
	v_exp_f32_e32 v16, v122
	v_fma_f32 v123, v17, s16, -v105
	v_exp_f32_e32 v17, v123
	global_store_dword v116, v2, s[10:11] offset:256
	global_store_dword v116, v3, s[10:11] offset:1044
	global_store_dword v116, v4, s[10:11] offset:1832
	global_store_dword v116, v5, s[10:11] offset:2620
	s_waitcnt lgkmcnt(0)
	v_mfma_f32_32x32x16_f16 v[18:33], v[86:89], v[70:73], v[18:33]
	global_store_dword v117, v6, s[10:11] offset:256
	global_store_dword v117, v7, s[10:11] offset:1044
	global_store_dword v117, v8, s[10:11] offset:1832
	global_store_dword v117, v9, s[10:11] offset:2620
	global_store_dword v118, v10, s[10:11] offset:256
	global_store_dword v118, v11, s[10:11] offset:1044
	global_store_dword v118, v12, s[10:11] offset:1832
	global_store_dword v118, v13, s[10:11] offset:2620
	global_store_dword v119, v14, s[10:11] offset:256
	global_store_dword v119, v15, s[10:11] offset:1044
	global_store_dword v119, v16, s[10:11] offset:1832
	global_store_dword v119, v17, s[10:11] offset:2620
	ds_read_b128 v[66:69], v112 offset:18432
	ds_read_b128 v[70:73], v112 offset:18464
	s_waitcnt lgkmcnt(1)
	v_mfma_f32_32x32x16_f16 v[2:17], v[74:77], v[66:69], 0
	v_fma_f32 v120, v18, s16, -v90
	v_exp_f32_e32 v18, v120
	v_fma_f32 v121, v19, s16, -v91
	v_exp_f32_e32 v19, v121
	v_fma_f32 v122, v20, s16, -v92
	v_exp_f32_e32 v20, v122
	v_fma_f32 v123, v21, s16, -v93
	v_exp_f32_e32 v21, v123
	v_fma_f32 v120, v22, s16, -v94
	v_exp_f32_e32 v22, v120
	v_fma_f32 v121, v23, s16, -v95
	v_exp_f32_e32 v23, v121
	ds_read_b128 v[66:69], v112 offset:18496
	s_waitcnt lgkmcnt(1)
	v_mfma_f32_32x32x16_f16 v[2:17], v[78:81], v[70:73], v[2:17]
	v_fma_f32 v122, v24, s16, -v96
	v_exp_f32_e32 v24, v122
	v_fma_f32 v123, v25, s16, -v97
	v_exp_f32_e32 v25, v123
	v_fma_f32 v120, v26, s16, -v98
	v_exp_f32_e32 v26, v120
	v_fma_f32 v121, v27, s16, -v99
	v_exp_f32_e32 v27, v121
	v_fma_f32 v122, v28, s16, -v100
	v_exp_f32_e32 v28, v122
	v_fma_f32 v123, v29, s16, -v101
	v_exp_f32_e32 v29, v123
	ds_read_b128 v[70:73], v112 offset:18528
	s_waitcnt lgkmcnt(1)
	v_mfma_f32_32x32x16_f16 v[2:17], v[82:85], v[66:69], v[2:17]
	v_fma_f32 v120, v30, s16, -v102
	v_exp_f32_e32 v30, v120
	v_fma_f32 v121, v31, s16, -v103
	v_exp_f32_e32 v31, v121
	v_fma_f32 v122, v32, s16, -v104
	v_exp_f32_e32 v32, v122
	v_fma_f32 v123, v33, s16, -v105
	v_exp_f32_e32 v33, v123
	global_store_dword v116, v18, s[10:11] offset:384
	global_store_dword v116, v19, s[10:11] offset:1172
	global_store_dword v116, v20, s[10:11] offset:1960
	global_store_dword v116, v21, s[10:11] offset:2748
	s_waitcnt lgkmcnt(0)
	v_mfma_f32_32x32x16_f16 v[2:17], v[86:89], v[70:73], v[2:17]
	global_store_dword v117, v22, s[10:11] offset:384
	global_store_dword v117, v23, s[10:11] offset:1172
	global_store_dword v117, v24, s[10:11] offset:1960
	global_store_dword v117, v25, s[10:11] offset:2748
	global_store_dword v118, v26, s[10:11] offset:384
	global_store_dword v118, v27, s[10:11] offset:1172
	global_store_dword v118, v28, s[10:11] offset:1960
	global_store_dword v118, v29, s[10:11] offset:2748
	global_store_dword v119, v30, s[10:11] offset:384
	global_store_dword v119, v31, s[10:11] offset:1172
	global_store_dword v119, v32, s[10:11] offset:1960
	global_store_dword v119, v33, s[10:11] offset:2748
	ds_read_b128 v[66:69], v112 offset:23040
	ds_read_b128 v[70:73], v112 offset:23072
	s_waitcnt lgkmcnt(1)
	v_mfma_f32_32x32x16_f16 v[18:33], v[74:77], v[66:69], 0
	v_fma_f32 v120, v2, s16, -v90
	v_exp_f32_e32 v2, v120
	v_fma_f32 v121, v3, s16, -v91
	v_exp_f32_e32 v3, v121
	v_fma_f32 v122, v4, s16, -v92
	v_exp_f32_e32 v4, v122
	v_fma_f32 v123, v5, s16, -v93
	v_exp_f32_e32 v5, v123
	v_fma_f32 v120, v6, s16, -v94
	v_exp_f32_e32 v6, v120
	v_fma_f32 v121, v7, s16, -v95
	v_exp_f32_e32 v7, v121
	ds_read_b128 v[66:69], v112 offset:23104
	s_waitcnt lgkmcnt(1)
	v_mfma_f32_32x32x16_f16 v[18:33], v[78:81], v[70:73], v[18:33]
	v_fma_f32 v122, v8, s16, -v96
	v_exp_f32_e32 v8, v122
	v_fma_f32 v123, v9, s16, -v97
	v_exp_f32_e32 v9, v123
	v_fma_f32 v120, v10, s16, -v98
	v_exp_f32_e32 v10, v120
	v_fma_f32 v121, v11, s16, -v99
	v_exp_f32_e32 v11, v121
	v_fma_f32 v122, v12, s16, -v100
	v_exp_f32_e32 v12, v122
	v_fma_f32 v123, v13, s16, -v101
	v_exp_f32_e32 v13, v123
	ds_read_b128 v[70:73], v112 offset:23136
	s_waitcnt lgkmcnt(1)
	v_mfma_f32_32x32x16_f16 v[18:33], v[82:85], v[66:69], v[18:33]
	v_fma_f32 v120, v14, s16, -v102
	v_exp_f32_e32 v14, v120
	v_fma_f32 v121, v15, s16, -v103
	v_exp_f32_e32 v15, v121
	v_fma_f32 v122, v16, s16, -v104
	v_exp_f32_e32 v16, v122
	v_fma_f32 v123, v17, s16, -v105
	v_exp_f32_e32 v17, v123
	global_store_dword v116, v2, s[10:11] offset:512
	global_store_dword v116, v3, s[10:11] offset:1300
	global_store_dword v116, v4, s[10:11] offset:2088
	global_store_dword v116, v5, s[10:11] offset:2876
	s_waitcnt lgkmcnt(0)
	v_mfma_f32_32x32x16_f16 v[18:33], v[86:89], v[70:73], v[18:33]
	global_store_dword v117, v6, s[10:11] offset:512
	global_store_dword v117, v7, s[10:11] offset:1300
	global_store_dword v117, v8, s[10:11] offset:2088
	global_store_dword v117, v9, s[10:11] offset:2876
	global_store_dword v118, v10, s[10:11] offset:512
	global_store_dword v118, v11, s[10:11] offset:1300
	global_store_dword v118, v12, s[10:11] offset:2088
	global_store_dword v118, v13, s[10:11] offset:2876
	global_store_dword v119, v14, s[10:11] offset:512
	global_store_dword v119, v15, s[10:11] offset:1300
	global_store_dword v119, v16, s[10:11] offset:2088
	global_store_dword v119, v17, s[10:11] offset:2876
	ds_read_b128 v[66:69], v112 offset:27648
	ds_read_b128 v[70:73], v112 offset:27680
	s_waitcnt lgkmcnt(1)
	v_mfma_f32_32x32x16_f16 v[2:17], v[74:77], v[66:69], 0
	v_fma_f32 v120, v18, s16, -v90
	v_exp_f32_e32 v18, v120
	v_fma_f32 v121, v19, s16, -v91
	v_exp_f32_e32 v19, v121
	v_fma_f32 v122, v20, s16, -v92
	v_exp_f32_e32 v20, v122
	v_fma_f32 v123, v21, s16, -v93
	v_exp_f32_e32 v21, v123
	v_fma_f32 v120, v22, s16, -v94
	v_exp_f32_e32 v22, v120
	v_fma_f32 v121, v23, s16, -v95
	v_exp_f32_e32 v23, v121
	ds_read_b128 v[66:69], v112 offset:27712
	s_waitcnt lgkmcnt(1)
	v_mfma_f32_32x32x16_f16 v[2:17], v[78:81], v[70:73], v[2:17]
	v_fma_f32 v122, v24, s16, -v96
	v_exp_f32_e32 v24, v122
	v_fma_f32 v123, v25, s16, -v97
	v_exp_f32_e32 v25, v123
	v_fma_f32 v120, v26, s16, -v98
	v_exp_f32_e32 v26, v120
	v_fma_f32 v121, v27, s16, -v99
	v_exp_f32_e32 v27, v121
	v_fma_f32 v122, v28, s16, -v100
	v_exp_f32_e32 v28, v122
	v_fma_f32 v123, v29, s16, -v101
	v_exp_f32_e32 v29, v123
	ds_read_b128 v[70:73], v112 offset:27744
	s_waitcnt lgkmcnt(1)
	v_mfma_f32_32x32x16_f16 v[2:17], v[82:85], v[66:69], v[2:17]
	v_fma_f32 v120, v30, s16, -v102
	v_exp_f32_e32 v30, v120
	v_fma_f32 v121, v31, s16, -v103
	v_exp_f32_e32 v31, v121
	v_fma_f32 v122, v32, s16, -v104
	v_exp_f32_e32 v32, v122
	v_fma_f32 v123, v33, s16, -v105
	v_exp_f32_e32 v33, v123
	global_store_dword v116, v18, s[10:11] offset:640
	global_store_dword v116, v19, s[10:11] offset:1428
	global_store_dword v116, v20, s[10:11] offset:2216
	global_store_dword v116, v21, s[10:11] offset:3004
	s_waitcnt lgkmcnt(0)
	v_mfma_f32_32x32x16_f16 v[2:17], v[86:89], v[70:73], v[2:17]
	global_store_dword v117, v22, s[10:11] offset:640
	global_store_dword v117, v23, s[10:11] offset:1428
	global_store_dword v117, v24, s[10:11] offset:2216
	global_store_dword v117, v25, s[10:11] offset:3004
	global_store_dword v118, v26, s[10:11] offset:640
	global_store_dword v118, v27, s[10:11] offset:1428
	global_store_dword v118, v28, s[10:11] offset:2216
	global_store_dword v118, v29, s[10:11] offset:3004
	global_store_dword v119, v30, s[10:11] offset:640
	global_store_dword v119, v31, s[10:11] offset:1428
	global_store_dword v119, v32, s[10:11] offset:2216
	global_store_dword v119, v33, s[10:11] offset:3004
	s_nop 15
	s_nop 1
	v_fma_f32 v120, v2, s16, -v90
	v_exp_f32_e32 v2, v120
	v_fma_f32 v121, v3, s16, -v91
	v_exp_f32_e32 v3, v121
	v_fma_f32 v122, v4, s16, -v92
	v_exp_f32_e32 v4, v122
	v_fma_f32 v123, v5, s16, -v93
	v_exp_f32_e32 v5, v123
	v_fma_f32 v120, v6, s16, -v94
	v_exp_f32_e32 v6, v120
	v_fma_f32 v121, v7, s16, -v95
	v_exp_f32_e32 v7, v121
	v_fma_f32 v122, v8, s16, -v96
	v_exp_f32_e32 v8, v122
	v_fma_f32 v123, v9, s16, -v97
	v_exp_f32_e32 v9, v123
	v_fma_f32 v120, v10, s16, -v98
	v_exp_f32_e32 v10, v120
	v_fma_f32 v121, v11, s16, -v99
	v_exp_f32_e32 v11, v121
	v_fma_f32 v122, v12, s16, -v100
	v_exp_f32_e32 v12, v122
	v_fma_f32 v123, v13, s16, -v101
	v_exp_f32_e32 v13, v123
	v_fma_f32 v120, v14, s16, -v102
	v_exp_f32_e32 v14, v120
	v_fma_f32 v121, v15, s16, -v103
	v_exp_f32_e32 v15, v121
	v_fma_f32 v122, v16, s16, -v104
	v_exp_f32_e32 v16, v122
	v_fma_f32 v123, v17, s16, -v105
	v_exp_f32_e32 v17, v123
	s_and_b64 exec, exec, s[22:23]
	global_store_dword v116, v2, s[10:11] offset:768
	global_store_dword v116, v3, s[10:11] offset:1556
	global_store_dword v116, v4, s[10:11] offset:2344
	global_store_dword v116, v5, s[10:11] offset:3132
	global_store_dword v117, v6, s[10:11] offset:768
	global_store_dword v117, v7, s[10:11] offset:1556
	global_store_dword v117, v8, s[10:11] offset:2344
	global_store_dword v117, v9, s[10:11] offset:3132
	global_store_dword v118, v10, s[10:11] offset:768
	global_store_dword v118, v11, s[10:11] offset:1556
	global_store_dword v118, v12, s[10:11] offset:2344
	global_store_dword v118, v13, s[10:11] offset:3132
	global_store_dword v119, v14, s[10:11] offset:768
	global_store_dword v119, v15, s[10:11] offset:1556
	global_store_dword v119, v16, s[10:11] offset:2344
	global_store_dword v119, v17, s[10:11] offset:3132
	s_mov_b64 exec, s[18:19]
	s_endpgm
